# v51 + spatial gating unit LayerNorm pass hand-written: rows software-pipelined two ahead (double-buffered LDS reads), natural packed pairs, same math order
# baseline (speedup 1.0000x reference)
; #define LAS __attribute__((address_space(3)))
; __device__ __forceinline__ unsigned pk2(float lo, float hi) { return f2bf(lo) | (f2bf(hi) << 16); }
; #define SPROBE(k) do { const unsigned long long tn_ = __builtin_amdgcn_s_memrealtime(); if (blockIdx.x == 0 && threadIdx.x == 0) atomicAdd(probe_words + (k), (unsigned)(tn_ - tp0_)); tp0_ = tn_; } while (0)
; #define SPROBE(k) do {} while (0)
; __device__ __forceinline__ void sgu_unit(LAS unsigned char* lds, int unit, const bf16* U, const bf16* VG, const bf16* Wsb, const float* bs, const float* lng, const float* lnb, bf16* YA, const float* stat, int tid_in, int lane_in, int wave, unsigned* probe_words = nullptr) {
;     ...
;         const int rsub = lane >> 5, ps = lane & 31;
; #pragma unroll
;         for (int i = 0; i < 8; ++i) { const int q = wave * 8 + i, row = 2 * q + rsub;
;             const bf16* src = VG + (row0 + row) * GW + half * 256 + ((ps ^ sgu_xkey(row)) * 8);
;             __builtin_amdgcn_global_load_lds((const unsigned*)src, (LAS unsigned*)(VS + q * 1024), 16, 0, 0); }
;     }
;     asm volatile("s_waitcnt vmcnt(0)" ::: "memory");
;     __syncthreads();
;     SPROBE(5);
;     {
;         const int pc = tid & 31, rb = tid >> 5;
;         const f32x4s ga = *(const LAS f32x4s*)(LG + pc * 8), gb = *(const LAS f32x4s*)(LG + pc * 8 + 4), ba = *(const LAS f32x4s*)(LB + pc * 8), bb = *(const LAS f32x4s*)(LB + pc * 8 + 4);
; #pragma unroll
;         for (int it = 0; it < 8; ++it) { const int jr = it * 16 + rb; const float mu = MU[jr], rs = RS[jr];
;             LAS v4u* cp = (LAS v4u*)(VS + jr * 512 + ((pc ^ sgu_xkey(jr)) * 16));
;             const v4u w = *cp; v4u o;
;             o.x = pk2((__uint_as_float(w.x << 16) - mu) * rs * ga[0] + ba[0], (__uint_as_float(w.x & 0xffff0000u) - mu) * rs * ga[1] + ba[1]);
;             o.y = pk2((__uint_as_float(w.y << 16) - mu) * rs * ga[2] + ba[2], (__uint_as_float(w.y & 0xffff0000u) - mu) * rs * ga[3] + ba[3]);
;             o.z = pk2((__uint_as_float(w.z << 16) - mu) * rs * gb[0] + bb[0], (__uint_as_float(w.z & 0xffff0000u) - mu) * rs * gb[1] + bb[1]);
;             o.w = pk2((__uint_as_float(w.w << 16) - mu) * rs * gb[2] + bb[2], (__uint_as_float(w.w & 0xffff0000u) - mu) * rs * gb[3] + bb[3]);
;             *cp = o; }
.LBB0_993:
	s_or_b64 exec, exec, s[0:1]
	v_lshl_add_u32 v70, v130, 2, 0
	v_lshrrev_b32_e32 v74, 5, v68
	s_waitcnt vmcnt(0)
	ds_write_b32 v70, v69 offset:1024
	v_or_b32_e32 v70, s35, v74
	v_ashrrev_i32_e32 v71, 31, v70
	v_and_b32_e32 v84, 31, v130
	v_lshl_add_u64 v[70:71], s[64:65], 0, v[70:71]
	v_lshlrev_b64 v[70:71], 10, v[70:71]
	v_lshlrev_b32_e32 v69, 4, v84
	v_lshl_add_u64 v[70:71], s[82:83], 0, v[70:71]
	v_bitop3_b32 v68, v68, v69, 32 bitop3:0x6c
	v_mov_b32_e32 v69, v3
	v_lshl_add_u64 v[70:71], v[70:71], 0, v[68:69]
	s_mov_b32 m0, s59
	v_readlane_b32 s0, v255, 41
	global_load_lds_dwordx4 v[70:71], off
	v_or_b32_e32 v70, s31, v74
	v_ashrrev_i32_e32 v71, 31, v70
	v_lshl_add_u64 v[72:73], s[64:65], 0, v[70:71]
	v_lshlrev_b32_e32 v70, 1, v70
	v_lshlrev_b64 v[72:73], 10, v[72:73]
	v_bitop3_b32 v70, v70, v84, 6 bitop3:0x6c
	v_lshl_add_u64 v[72:73], s[82:83], 0, v[72:73]
	v_lshlrev_b32_e32 v70, 4, v70
	v_mov_b32_e32 v71, v3
	v_lshl_add_u64 v[70:71], v[72:73], 0, v[70:71]
	s_mov_b32 m0, s92
	v_ashrrev_i32_e32 v85, 5, v130
	global_load_lds_dwordx4 v[70:71], off
	v_or_b32_e32 v70, s88, v74
	v_ashrrev_i32_e32 v71, 31, v70
	v_lshl_add_u64 v[70:71], s[64:65], 0, v[70:71]
	v_lshlrev_b64 v[70:71], 10, v[70:71]
	v_lshl_add_u64 v[70:71], s[82:83], 0, v[70:71]
	v_lshl_add_u64 v[68:69], v[70:71], 0, v[68:69]
	s_mov_b32 m0, s94
	v_lshlrev_b32_e32 v86, 1, v85
	global_load_lds_dwordx4 v[68:69], off
	v_or_b32_e32 v68, s58, v74
	v_ashrrev_i32_e32 v69, 31, v68
	v_lshl_add_u64 v[70:71], s[64:65], 0, v[68:69]
	v_lshlrev_b32_e32 v68, 1, v68
	v_lshlrev_b64 v[70:71], 10, v[70:71]
	v_bitop3_b32 v68, v68, v84, 6 bitop3:0x6c
	v_lshl_add_u64 v[70:71], s[82:83], 0, v[70:71]
	v_lshlrev_b32_e32 v68, 4, v68
	v_mov_b32_e32 v69, v3
	v_lshl_add_u64 v[68:69], v[70:71], 0, v[68:69]
	s_mov_b32 m0, s96
	v_lshlrev_b32_e32 v70, 1, v74
	global_load_lds_dwordx4 v[68:69], off
	v_or_b32_e32 v68, s89, v74
	v_ashrrev_i32_e32 v69, 31, v68
	v_lshl_add_u64 v[68:69], s[64:65], 0, v[68:69]
	v_lshlrev_b64 v[68:69], 10, v[68:69]
	v_bitop3_b32 v70, v70, v84, 8 bitop3:0x36
	v_lshl_add_u64 v[68:69], s[82:83], 0, v[68:69]
	v_lshlrev_b32_e32 v70, 4, v70
	v_mov_b32_e32 v71, v3
	v_lshl_add_u64 v[68:69], v[68:69], 0, v[70:71]
	s_mov_b32 m0, s0
	v_readlane_b32 s0, v255, 42
	global_load_lds_dwordx4 v[68:69], off
	v_or_b32_e32 v68, s84, v74
	v_ashrrev_i32_e32 v69, 31, v68
	v_lshl_add_u64 v[72:73], s[64:65], 0, v[68:69]
	v_lshlrev_b32_e32 v68, 1, v68
	v_and_b32_e32 v68, 6, v68
	v_lshlrev_b64 v[72:73], 10, v[72:73]
	v_bitop3_b32 v68, v68, v84, 8 bitop3:0x36
	v_lshl_add_u64 v[72:73], s[82:83], 0, v[72:73]
	v_lshlrev_b32_e32 v68, 4, v68
	v_mov_b32_e32 v69, v3
	v_lshl_add_u64 v[68:69], v[72:73], 0, v[68:69]
	s_mov_b32 m0, s0
	v_readlane_b32 s0, v255, 31
	global_load_lds_dwordx4 v[68:69], off
	v_or_b32_e32 v68, s85, v74
	v_ashrrev_i32_e32 v69, 31, v68
	v_lshl_add_u64 v[68:69], s[64:65], 0, v[68:69]
	v_lshlrev_b64 v[68:69], 10, v[68:69]
	v_lshl_add_u64 v[68:69], s[82:83], 0, v[68:69]
	v_lshl_add_u64 v[68:69], v[68:69], 0, v[70:71]
	s_mov_b32 m0, s0
	v_and_b32_e32 v86, 6, v86
	global_load_lds_dwordx4 v[68:69], off
	v_or_b32_e32 v68, s38, v74
	v_ashrrev_i32_e32 v69, 31, v68
	v_lshl_add_u64 v[70:71], s[64:65], 0, v[68:69]
	v_lshlrev_b32_e32 v68, 1, v68
	v_lshlrev_b64 v[70:71], 10, v[70:71]
	v_bitop3_b32 v68, v68, v84, 14 bitop3:0x6c
	v_and_b32_e32 v87, 8, v85
	v_lshl_add_u64 v[70:71], s[82:83], 0, v[70:71]
	v_lshlrev_b32_e32 v68, 4, v68
	v_mov_b32_e32 v69, v3
	v_readlane_b32 s0, v255, 18
	v_lshl_add_u32 v72, v84, 5, 0
	v_bitop3_b32 v84, v86, v84, v87 bitop3:0x36
	v_lshl_add_u64 v[68:69], v[70:71], 0, v[68:69]
	s_mov_b32 m0, s0
	v_lshlrev_b32_e32 v87, 4, v84
	v_lshl_add_u32 v84, v85, 2, 0
	v_lshlrev_b32_e32 v85, 9, v85
	global_load_lds_dwordx4 v[68:69], off
	v_add3_u32 v132, 0, v87, v85
	s_waitcnt vmcnt(0)
	s_waitcnt vmcnt(0) lgkmcnt(0)
	s_barrier
	s_movk_i32 s0, 0x60
	s_and_b64 vcc, exec, s[10:11]
	ds_read_b128 v[76:79], v72 offset:1024
	ds_read_b128 v[68:71], v72 offset:1040
	ds_read_b128 v[80:83], v72 offset:2048
	ds_read_b128 v[72:75], v72 offset:2064
	ds_read_b32 v86, v84
	ds_read_b32 v138, v84 offset:512
	ds_read_b128 v[134:137], v132 offset:4096
	ds_read_b32 v150, v84 offset:64
	ds_read_b32 v152, v84 offset:576
	ds_read_b128 v[144:147], v132 offset:12288
	s_waitcnt lgkmcnt(3)
	v_lshlrev_b32_e32 v156, 16, v134
	v_and_b32_e32 v157, 0xffff0000, v134
	v_lshlrev_b32_e32 v158, 16, v135
	v_and_b32_e32 v159, 0xffff0000, v135
	v_lshlrev_b32_e32 v160, 16, v136
	v_and_b32_e32 v161, 0xffff0000, v136
	v_lshlrev_b32_e32 v162, 16, v137
	v_and_b32_e32 v163, 0xffff0000, v137
	v_pk_add_f32 v[156:157], v[156:157], v[86:87] op_sel_hi:[1,0] neg_lo:[0,1] neg_hi:[0,1]
	v_pk_add_f32 v[158:159], v[158:159], v[86:87] op_sel_hi:[1,0] neg_lo:[0,1] neg_hi:[0,1]
	v_pk_add_f32 v[160:161], v[160:161], v[86:87] op_sel_hi:[1,0] neg_lo:[0,1] neg_hi:[0,1]
	v_pk_add_f32 v[162:163], v[162:163], v[86:87] op_sel_hi:[1,0] neg_lo:[0,1] neg_hi:[0,1]
	v_pk_mul_f32 v[156:157], v[138:139], v[156:157] op_sel_hi:[0,1]
	v_pk_mul_f32 v[158:159], v[138:139], v[158:159] op_sel_hi:[0,1]
	v_pk_mul_f32 v[160:161], v[138:139], v[160:161] op_sel_hi:[0,1]
	v_pk_mul_f32 v[162:163], v[138:139], v[162:163] op_sel_hi:[0,1]
	v_pk_fma_f32 v[156:157], v[76:77], v[156:157], v[80:81]
	v_pk_fma_f32 v[158:159], v[78:79], v[158:159], v[82:83]
	v_pk_fma_f32 v[160:161], v[68:69], v[160:161], v[72:73]
	v_pk_fma_f32 v[162:163], v[70:71], v[162:163], v[74:75]
	v_cvt_pk_bf16_f32 v140, v156, v157
	v_cvt_pk_bf16_f32 v141, v158, v159
	v_cvt_pk_bf16_f32 v142, v160, v161
	v_cvt_pk_bf16_f32 v143, v162, v163
	ds_write_b128 v132, v[140:143] offset:4096
	ds_read_b32 v86, v84 offset:128
	ds_read_b32 v138, v84 offset:640
	ds_read_b128 v[134:137], v132 offset:20480
	s_waitcnt lgkmcnt(4)
; #define LAS __attribute__((address_space(3)))
; __device__ __forceinline__ unsigned pk2(float lo, float hi) { return f2bf(lo) | (f2bf(hi) << 16); }
; __device__ __forceinline__ void sgu_unit(LAS unsigned char* lds, int unit, const bf16* U, const bf16* VG, const bf16* Wsb, const float* bs, const float* lng, const float* lnb, bf16* YA, const float* stat, int tid_in, int lane_in, int wave, unsigned* probe_words = nullptr) {
;     ...
;         const int pc = tid & 31, rb = tid >> 5;
;         const f32x4s ga = *(const LAS f32x4s*)(LG + pc * 8), gb = *(const LAS f32x4s*)(LG + pc * 8 + 4), ba = *(const LAS f32x4s*)(LB + pc * 8), bb = *(const LAS f32x4s*)(LB + pc * 8 + 4);
; #pragma unroll
;         for (int it = 0; it < 8; ++it) { const int jr = it * 16 + rb; const float mu = MU[jr], rs = RS[jr];
;             LAS v4u* cp = (LAS v4u*)(VS + jr * 512 + ((pc ^ sgu_xkey(jr)) * 16));
;             const v4u w = *cp; v4u o;
;             o.x = pk2((__uint_as_float(w.x << 16) - mu) * rs * ga[0] + ba[0], (__uint_as_float(w.x & 0xffff0000u) - mu) * rs * ga[1] + ba[1]);
;             o.y = pk2((__uint_as_float(w.y << 16) - mu) * rs * ga[2] + ba[2], (__uint_as_float(w.y & 0xffff0000u) - mu) * rs * ga[3] + ba[3]);
;             o.z = pk2((__uint_as_float(w.z << 16) - mu) * rs * gb[0] + bb[0], (__uint_as_float(w.z & 0xffff0000u) - mu) * rs * gb[1] + bb[1]);
;             o.w = pk2((__uint_as_float(w.w << 16) - mu) * rs * gb[2] + bb[2], (__uint_as_float(w.w & 0xffff0000u) - mu) * rs * gb[3] + bb[3]);
;             *cp = o; }
	v_lshlrev_b32_e32 v156, 16, v144
	v_and_b32_e32 v157, 0xffff0000, v144
	v_lshlrev_b32_e32 v158, 16, v145
	v_and_b32_e32 v159, 0xffff0000, v145
	v_lshlrev_b32_e32 v160, 16, v146
	v_and_b32_e32 v161, 0xffff0000, v146
	v_lshlrev_b32_e32 v162, 16, v147
	v_and_b32_e32 v163, 0xffff0000, v147
	v_pk_add_f32 v[156:157], v[156:157], v[150:151] op_sel_hi:[1,0] neg_lo:[0,1] neg_hi:[0,1]
	v_pk_add_f32 v[158:159], v[158:159], v[150:151] op_sel_hi:[1,0] neg_lo:[0,1] neg_hi:[0,1]
	v_pk_add_f32 v[160:161], v[160:161], v[150:151] op_sel_hi:[1,0] neg_lo:[0,1] neg_hi:[0,1]
	v_pk_add_f32 v[162:163], v[162:163], v[150:151] op_sel_hi:[1,0] neg_lo:[0,1] neg_hi:[0,1]
	v_pk_mul_f32 v[156:157], v[152:153], v[156:157] op_sel_hi:[0,1]
	v_pk_mul_f32 v[158:159], v[152:153], v[158:159] op_sel_hi:[0,1]
	v_pk_mul_f32 v[160:161], v[152:153], v[160:161] op_sel_hi:[0,1]
	v_pk_mul_f32 v[162:163], v[152:153], v[162:163] op_sel_hi:[0,1]
	v_pk_fma_f32 v[156:157], v[76:77], v[156:157], v[80:81]
	v_pk_fma_f32 v[158:159], v[78:79], v[158:159], v[82:83]
	v_pk_fma_f32 v[160:161], v[68:69], v[160:161], v[72:73]
	v_pk_fma_f32 v[162:163], v[70:71], v[162:163], v[74:75]
	v_cvt_pk_bf16_f32 v164, v156, v157
	v_cvt_pk_bf16_f32 v165, v158, v159
	v_cvt_pk_bf16_f32 v166, v160, v161
	v_cvt_pk_bf16_f32 v167, v162, v163
	ds_write_b128 v132, v[164:167] offset:12288
	ds_read_b32 v150, v84 offset:192
	ds_read_b32 v152, v84 offset:704
	ds_read_b128 v[144:147], v132 offset:28672
	s_waitcnt lgkmcnt(4)
	v_lshlrev_b32_e32 v156, 16, v134
	v_and_b32_e32 v157, 0xffff0000, v134
	v_lshlrev_b32_e32 v158, 16, v135
	v_and_b32_e32 v159, 0xffff0000, v135
	v_lshlrev_b32_e32 v160, 16, v136
	v_and_b32_e32 v161, 0xffff0000, v136
	v_lshlrev_b32_e32 v162, 16, v137
	v_and_b32_e32 v163, 0xffff0000, v137
	v_pk_add_f32 v[156:157], v[156:157], v[86:87] op_sel_hi:[1,0] neg_lo:[0,1] neg_hi:[0,1]
	v_pk_add_f32 v[158:159], v[158:159], v[86:87] op_sel_hi:[1,0] neg_lo:[0,1] neg_hi:[0,1]
	v_pk_add_f32 v[160:161], v[160:161], v[86:87] op_sel_hi:[1,0] neg_lo:[0,1] neg_hi:[0,1]
	v_pk_add_f32 v[162:163], v[162:163], v[86:87] op_sel_hi:[1,0] neg_lo:[0,1] neg_hi:[0,1]
	v_pk_mul_f32 v[156:157], v[138:139], v[156:157] op_sel_hi:[0,1]
	v_pk_mul_f32 v[158:159], v[138:139], v[158:159] op_sel_hi:[0,1]
	v_pk_mul_f32 v[160:161], v[138:139], v[160:161] op_sel_hi:[0,1]
	v_pk_mul_f32 v[162:163], v[138:139], v[162:163] op_sel_hi:[0,1]
	v_pk_fma_f32 v[156:157], v[76:77], v[156:157], v[80:81]
	v_pk_fma_f32 v[158:159], v[78:79], v[158:159], v[82:83]
	v_pk_fma_f32 v[160:161], v[68:69], v[160:161], v[72:73]
	v_pk_fma_f32 v[162:163], v[70:71], v[162:163], v[74:75]
	v_cvt_pk_bf16_f32 v140, v156, v157
	v_cvt_pk_bf16_f32 v141, v158, v159
	v_cvt_pk_bf16_f32 v142, v160, v161
	v_cvt_pk_bf16_f32 v143, v162, v163
	ds_write_b128 v132, v[140:143] offset:20480
	ds_read_b32 v86, v84 offset:256
	ds_read_b32 v138, v84 offset:768
	ds_read_b128 v[134:137], v132 offset:36864
	s_waitcnt lgkmcnt(4)
	v_lshlrev_b32_e32 v156, 16, v144
	v_and_b32_e32 v157, 0xffff0000, v144
	v_lshlrev_b32_e32 v158, 16, v145
	v_and_b32_e32 v159, 0xffff0000, v145
	v_lshlrev_b32_e32 v160, 16, v146
	v_and_b32_e32 v161, 0xffff0000, v146
	v_lshlrev_b32_e32 v162, 16, v147
	v_and_b32_e32 v163, 0xffff0000, v147
	v_pk_add_f32 v[156:157], v[156:157], v[150:151] op_sel_hi:[1,0] neg_lo:[0,1] neg_hi:[0,1]
	v_pk_add_f32 v[158:159], v[158:159], v[150:151] op_sel_hi:[1,0] neg_lo:[0,1] neg_hi:[0,1]
	v_pk_add_f32 v[160:161], v[160:161], v[150:151] op_sel_hi:[1,0] neg_lo:[0,1] neg_hi:[0,1]
	v_pk_add_f32 v[162:163], v[162:163], v[150:151] op_sel_hi:[1,0] neg_lo:[0,1] neg_hi:[0,1]
	v_pk_mul_f32 v[156:157], v[152:153], v[156:157] op_sel_hi:[0,1]
	v_pk_mul_f32 v[158:159], v[152:153], v[158:159] op_sel_hi:[0,1]
	v_pk_mul_f32 v[160:161], v[152:153], v[160:161] op_sel_hi:[0,1]
	v_pk_mul_f32 v[162:163], v[152:153], v[162:163] op_sel_hi:[0,1]
	v_pk_fma_f32 v[156:157], v[76:77], v[156:157], v[80:81]
	v_pk_fma_f32 v[158:159], v[78:79], v[158:159], v[82:83]
	v_pk_fma_f32 v[160:161], v[68:69], v[160:161], v[72:73]
	v_pk_fma_f32 v[162:163], v[70:71], v[162:163], v[74:75]
	v_cvt_pk_bf16_f32 v164, v156, v157
	v_cvt_pk_bf16_f32 v165, v158, v159
	v_cvt_pk_bf16_f32 v166, v160, v161
	v_cvt_pk_bf16_f32 v167, v162, v163
	ds_write_b128 v132, v[164:167] offset:28672
	ds_read_b32 v150, v84 offset:320
	ds_read_b32 v152, v84 offset:832
	ds_read_b128 v[144:147], v132 offset:45056
	s_waitcnt lgkmcnt(4)
	v_lshlrev_b32_e32 v156, 16, v134
	v_and_b32_e32 v157, 0xffff0000, v134
	v_lshlrev_b32_e32 v158, 16, v135
	v_and_b32_e32 v159, 0xffff0000, v135
	v_lshlrev_b32_e32 v160, 16, v136
	v_and_b32_e32 v161, 0xffff0000, v136
	v_lshlrev_b32_e32 v162, 16, v137
	v_and_b32_e32 v163, 0xffff0000, v137
	v_pk_add_f32 v[156:157], v[156:157], v[86:87] op_sel_hi:[1,0] neg_lo:[0,1] neg_hi:[0,1]
	v_pk_add_f32 v[158:159], v[158:159], v[86:87] op_sel_hi:[1,0] neg_lo:[0,1] neg_hi:[0,1]
	v_pk_add_f32 v[160:161], v[160:161], v[86:87] op_sel_hi:[1,0] neg_lo:[0,1] neg_hi:[0,1]
	v_pk_add_f32 v[162:163], v[162:163], v[86:87] op_sel_hi:[1,0] neg_lo:[0,1] neg_hi:[0,1]
	v_pk_mul_f32 v[156:157], v[138:139], v[156:157] op_sel_hi:[0,1]
	v_pk_mul_f32 v[158:159], v[138:139], v[158:159] op_sel_hi:[0,1]
	v_pk_mul_f32 v[160:161], v[138:139], v[160:161] op_sel_hi:[0,1]
	v_pk_mul_f32 v[162:163], v[138:139], v[162:163] op_sel_hi:[0,1]
	v_pk_fma_f32 v[156:157], v[76:77], v[156:157], v[80:81]
	v_pk_fma_f32 v[158:159], v[78:79], v[158:159], v[82:83]
	v_pk_fma_f32 v[160:161], v[68:69], v[160:161], v[72:73]
	v_pk_fma_f32 v[162:163], v[70:71], v[162:163], v[74:75]
	v_cvt_pk_bf16_f32 v140, v156, v157
	v_cvt_pk_bf16_f32 v141, v158, v159
	v_cvt_pk_bf16_f32 v142, v160, v161
	v_cvt_pk_bf16_f32 v143, v162, v163
	ds_write_b128 v132, v[140:143] offset:36864
	ds_read_b32 v86, v84 offset:384
	ds_read_b32 v138, v84 offset:896
	ds_read_b128 v[134:137], v132 offset:53248
	s_waitcnt lgkmcnt(4)
; #define LAS __attribute__((address_space(3)))
; __device__ __forceinline__ unsigned pk2(float lo, float hi) { return f2bf(lo) | (f2bf(hi) << 16); }
; __device__ __forceinline__ void sgu_unit(LAS unsigned char* lds, int unit, const bf16* U, const bf16* VG, const bf16* Wsb, const float* bs, const float* lng, const float* lnb, bf16* YA, const float* stat, int tid_in, int lane_in, int wave, unsigned* probe_words = nullptr) {
;     ...
;         const int pc = tid & 31, rb = tid >> 5;
;         const f32x4s ga = *(const LAS f32x4s*)(LG + pc * 8), gb = *(const LAS f32x4s*)(LG + pc * 8 + 4), ba = *(const LAS f32x4s*)(LB + pc * 8), bb = *(const LAS f32x4s*)(LB + pc * 8 + 4);
; #pragma unroll
;         for (int it = 0; it < 8; ++it) { const int jr = it * 16 + rb; const float mu = MU[jr], rs = RS[jr];
;             LAS v4u* cp = (LAS v4u*)(VS + jr * 512 + ((pc ^ sgu_xkey(jr)) * 16));
;             const v4u w = *cp; v4u o;
;             o.x = pk2((__uint_as_float(w.x << 16) - mu) * rs * ga[0] + ba[0], (__uint_as_float(w.x & 0xffff0000u) - mu) * rs * ga[1] + ba[1]);
;             o.y = pk2((__uint_as_float(w.y << 16) - mu) * rs * ga[2] + ba[2], (__uint_as_float(w.y & 0xffff0000u) - mu) * rs * ga[3] + ba[3]);
;             o.z = pk2((__uint_as_float(w.z << 16) - mu) * rs * gb[0] + bb[0], (__uint_as_float(w.z & 0xffff0000u) - mu) * rs * gb[1] + bb[1]);
;             o.w = pk2((__uint_as_float(w.w << 16) - mu) * rs * gb[2] + bb[2], (__uint_as_float(w.w & 0xffff0000u) - mu) * rs * gb[3] + bb[3]);
;             *cp = o; }
;     ...
;     {
;         const int tq = (lane & 15) >> 2, tp = lane & 3; const int xkp = sgu_xkey(8 * q4 + tq) ^ (tp >> 1);
;         const LAS unsigned char* tb = VS + (8 * q4 + tq) * 512 + 8 * (tp & 1);
; #pragma unroll
;         for (int gi = 0; gi < 4; ++gi) {
;             const int g = half * 4 + gi;
;             f32x4s acc[4];
; #pragma unroll
;             for (int nn = 0; nn < 4; ++nn) acc[nn] = (f32x4s){0.f, 0.f, 0.f, 0.f};
	v_lshlrev_b32_e32 v156, 16, v144
	v_and_b32_e32 v157, 0xffff0000, v144
	v_lshlrev_b32_e32 v158, 16, v145
	v_and_b32_e32 v159, 0xffff0000, v145
	v_lshlrev_b32_e32 v160, 16, v146
	v_and_b32_e32 v161, 0xffff0000, v146
	v_lshlrev_b32_e32 v162, 16, v147
	v_and_b32_e32 v163, 0xffff0000, v147
	v_pk_add_f32 v[156:157], v[156:157], v[150:151] op_sel_hi:[1,0] neg_lo:[0,1] neg_hi:[0,1]
	v_pk_add_f32 v[158:159], v[158:159], v[150:151] op_sel_hi:[1,0] neg_lo:[0,1] neg_hi:[0,1]
	v_pk_add_f32 v[160:161], v[160:161], v[150:151] op_sel_hi:[1,0] neg_lo:[0,1] neg_hi:[0,1]
	v_pk_add_f32 v[162:163], v[162:163], v[150:151] op_sel_hi:[1,0] neg_lo:[0,1] neg_hi:[0,1]
	v_pk_mul_f32 v[156:157], v[152:153], v[156:157] op_sel_hi:[0,1]
	v_pk_mul_f32 v[158:159], v[152:153], v[158:159] op_sel_hi:[0,1]
	v_pk_mul_f32 v[160:161], v[152:153], v[160:161] op_sel_hi:[0,1]
	v_pk_mul_f32 v[162:163], v[152:153], v[162:163] op_sel_hi:[0,1]
	v_pk_fma_f32 v[156:157], v[76:77], v[156:157], v[80:81]
	v_pk_fma_f32 v[158:159], v[78:79], v[158:159], v[82:83]
	v_pk_fma_f32 v[160:161], v[68:69], v[160:161], v[72:73]
	v_pk_fma_f32 v[162:163], v[70:71], v[162:163], v[74:75]
	v_cvt_pk_bf16_f32 v164, v156, v157
	v_cvt_pk_bf16_f32 v165, v158, v159
	v_cvt_pk_bf16_f32 v166, v160, v161
	v_cvt_pk_bf16_f32 v167, v162, v163
	ds_write_b128 v132, v[164:167] offset:45056
	ds_read_b32 v150, v84 offset:448
	ds_read_b32 v152, v84 offset:960
	ds_read_b128 v[144:147], v132 offset:61440
	s_waitcnt lgkmcnt(4)
	v_lshlrev_b32_e32 v156, 16, v134
	v_and_b32_e32 v157, 0xffff0000, v134
	v_lshlrev_b32_e32 v158, 16, v135
	v_and_b32_e32 v159, 0xffff0000, v135
	v_lshlrev_b32_e32 v160, 16, v136
	v_and_b32_e32 v161, 0xffff0000, v136
	v_lshlrev_b32_e32 v162, 16, v137
	v_and_b32_e32 v163, 0xffff0000, v137
	v_pk_add_f32 v[156:157], v[156:157], v[86:87] op_sel_hi:[1,0] neg_lo:[0,1] neg_hi:[0,1]
	v_pk_add_f32 v[158:159], v[158:159], v[86:87] op_sel_hi:[1,0] neg_lo:[0,1] neg_hi:[0,1]
	v_pk_add_f32 v[160:161], v[160:161], v[86:87] op_sel_hi:[1,0] neg_lo:[0,1] neg_hi:[0,1]
	v_pk_add_f32 v[162:163], v[162:163], v[86:87] op_sel_hi:[1,0] neg_lo:[0,1] neg_hi:[0,1]
	v_pk_mul_f32 v[156:157], v[138:139], v[156:157] op_sel_hi:[0,1]
	v_pk_mul_f32 v[158:159], v[138:139], v[158:159] op_sel_hi:[0,1]
	v_pk_mul_f32 v[160:161], v[138:139], v[160:161] op_sel_hi:[0,1]
	v_pk_mul_f32 v[162:163], v[138:139], v[162:163] op_sel_hi:[0,1]
	v_pk_fma_f32 v[156:157], v[76:77], v[156:157], v[80:81]
	v_pk_fma_f32 v[158:159], v[78:79], v[158:159], v[82:83]
	v_pk_fma_f32 v[160:161], v[68:69], v[160:161], v[72:73]
	v_pk_fma_f32 v[162:163], v[70:71], v[162:163], v[74:75]
	v_cvt_pk_bf16_f32 v140, v156, v157
	v_cvt_pk_bf16_f32 v141, v158, v159
	v_cvt_pk_bf16_f32 v142, v160, v161
	v_cvt_pk_bf16_f32 v143, v162, v163
	ds_write_b128 v132, v[140:143] offset:53248
	s_waitcnt lgkmcnt(1)
	v_lshlrev_b32_e32 v156, 16, v144
	v_and_b32_e32 v157, 0xffff0000, v144
	v_lshlrev_b32_e32 v158, 16, v145
	v_and_b32_e32 v159, 0xffff0000, v145
	v_lshlrev_b32_e32 v160, 16, v146
	v_and_b32_e32 v161, 0xffff0000, v146
	v_lshlrev_b32_e32 v162, 16, v147
	v_and_b32_e32 v163, 0xffff0000, v147
	v_pk_add_f32 v[156:157], v[156:157], v[150:151] op_sel_hi:[1,0] neg_lo:[0,1] neg_hi:[0,1]
	v_pk_add_f32 v[158:159], v[158:159], v[150:151] op_sel_hi:[1,0] neg_lo:[0,1] neg_hi:[0,1]
	v_pk_add_f32 v[160:161], v[160:161], v[150:151] op_sel_hi:[1,0] neg_lo:[0,1] neg_hi:[0,1]
	v_pk_add_f32 v[162:163], v[162:163], v[150:151] op_sel_hi:[1,0] neg_lo:[0,1] neg_hi:[0,1]
	v_pk_mul_f32 v[156:157], v[152:153], v[156:157] op_sel_hi:[0,1]
	v_pk_mul_f32 v[158:159], v[152:153], v[158:159] op_sel_hi:[0,1]
	v_pk_mul_f32 v[160:161], v[152:153], v[160:161] op_sel_hi:[0,1]
	v_pk_mul_f32 v[162:163], v[152:153], v[162:163] op_sel_hi:[0,1]
	v_pk_fma_f32 v[156:157], v[76:77], v[156:157], v[80:81]
	v_pk_fma_f32 v[158:159], v[78:79], v[158:159], v[82:83]
	v_pk_fma_f32 v[160:161], v[68:69], v[160:161], v[72:73]
	v_pk_fma_f32 v[162:163], v[70:71], v[162:163], v[74:75]
	v_cvt_pk_bf16_f32 v164, v156, v157
	v_cvt_pk_bf16_f32 v165, v158, v159
	v_cvt_pk_bf16_f32 v166, v160, v161
	v_cvt_pk_bf16_f32 v167, v162, v163
	ds_write_b128 v132, v[164:167] offset:61440
	v_lshrrev_b32_e32 v68, 2, v131
	v_or_b32_e32 v69, v2, v68
	v_lshlrev_b32_e32 v68, 1, v68
	v_and_b32_e32 v2, 8, v2
	v_bfe_u32 v70, v130, 1, 1
	v_or3_b32 v2, v2, v68, v70
	v_lshlrev_b32_e32 v68, 9, v69
	v_lshlrev_b32_e32 v69, 3, v130
	v_and_b32_e32 v69, 8, v69
	v_add3_u32 v125, 0, v68, v69
	v_mov_b32_e32 v84, 0
	v_lshlrev_b32_e32 v130, 4, v2
	v_add_u32_e32 v124, v125, v130
	v_xad_u32 v123, v130, 32, v125
	v_xad_u32 v122, v130, 64, v125
	v_xad_u32 v2, v130, s0, v125
	v_mov_b32_e32 v85, 0
	v_mov_b32_e32 v86, 0
	v_mov_b32_e32 v87, 0
	v_mov_b32_e32 v76, 0
	v_mov_b32_e32 v77, v84
	v_mov_b32_e32 v78, v84
	v_mov_b32_e32 v79, v84
	v_mov_b32_e32 v72, v84
	v_mov_b32_e32 v73, v84
	v_mov_b32_e32 v74, v84
	v_mov_b32_e32 v75, v84
	v_mov_b32_e32 v68, v84
	v_mov_b32_e32 v69, v84
	v_mov_b32_e32 v70, v84
	v_mov_b32_e32 v71, v84
	v_mov_b32_e32 v80, v84
	v_mov_b32_e32 v81, v84
	v_mov_b32_e32 v82, v84
	v_mov_b32_e32 v83, v84
	s_waitcnt lgkmcnt(0)
	s_barrier
	s_cbranch_vccz .LBB0_1016
	s_and_b64 vcc, exec, s[8:9]
	s_cbranch_vccz .LBB0_1017
